# hg_c direction-1: forward-output/gate loads issued right after the chunk-top wait instead of mid-chunk with an immediate vmcnt(0)
# speedup vs baseline: 1.0063x; 1.0063x over previous
; template <bool WITHO, bool RAW = false>
; __device__ __forceinline__ void hg_pass(const Frame& F, const bf16_t* P, const float* lbh, int b, int h, int nb, int dir, f32x4 (&S)[4][4], float (&Gsum)[16],
;                                         LAS bf16_t* Vl, LAS bf16_t* Kl, float* OF, const float* ngp) {
;     ...
;         for (int m = 0; m < 4; ++m) { const float z0 = __uint_as_float(zr[m].x << 16), z1 = __uint_as_float(zr[m].x & 0xffff0000u), z2 = __uint_as_float(zr[m].y << 16), z3 = __uint_as_float(zr[m].y & 0xffff0000u);
;             const float zz[4] = {z0, z1, z2, z3};
;             const f32x4 lb4 = *(const f32x4*)(lbh + 16 * m + 4 * g);
; #pragma unroll
;             for (int i = 0; i < 4; ++i) { const float lb = lb4[i]; const float f = fmaxf(lb + (1.0f - lb) * sigmoidf_(zz[i]), 1e-30f); kk[m * 4 + i] = 1.0f - f; c[m * 4 + i] = __logf(f); }
;             *(LAS u32x2*)(Vl + tau * 64 + 16 * m + 4 * g) = vr[m];
;  }
;         if (ci + 1 < HG_U / 16) { const int pos = (ci + 1) * 16 + tau, t = dir ? (HG_U - 1 - pos) : pos; const bf16_t* pr = P + (size_t)hg_row(b, nb, t) * 4096 + h * 64 + 4 * g;
; #pragma unroll
;             for (int m = 0; m < 4; ++m) { zr[m] = *(const u32x2*)(pr + (dir ? 2560 : 2048) + 16 * m); vr[m] = *(const u32x2*)(pr + 3072 + 16 * m); } }
;         float G[16];
; #pragma unroll
;         for (int q = 0; q < 16; ++q) G[q] = c[q];
; #pragma unroll
;         for (int q = 0; q < 16; q += 4) ROW_ALLREDUCE4(G[q], G[q + 1], G[q + 2], G[q + 3]);
; #pragma unroll
;         for (int q = 0; q < 16; ++q) { c[q] = dpp_add0<0x111>(c[q]); c[q] = dpp_add0<0x112>(c[q]); c[q] = dpp_add0<0x114>(c[q]); c[q] = dpp_add0<0x118>(c[q]); }
; #pragma unroll
;         for (int q = 0; q < 16; ++q) Gsum[q] += G[q];
; #pragma unroll
;         for (int m = 0; m < 4; ++m) { float kh[4];
; #pragma unroll
;             for (int i = 0; i < 4; ++i) kh[i] = kk[m * 4 + i] * __expf(G[m * 4 + i] - c[m * 4 + i]);
;             u32x2 w; w.x = cvt_pk_bf16(kh[0], kh[1]); w.y = cvt_pk_bf16(kh[2], kh[3]);
;             *(LAS u32x2*)(Kl + tau * 64 + 16 * m + 4 * g) = w; }
;         float ofv[4][4], gtv[4][4]; int orow[4];
;         if (WITHO) {
; #pragma unroll
;             for (int i = 0; i < 4; ++i) { const int p2 = ci * 16 + 4 * g + i, t2 = dir ? (HG_U - 1 - p2) : p2; orow[i] = hg_row(b, nb, t2); }
;             if (dir && !RAW) {
; #pragma unroll
.LBB0_1172:
	v_lshlrev_b32_e32 v3, 16, v90
	v_mul_f32_e32 v3, 0xbfb8aa3b, v3
	v_exp_f32_e32 v3, v3
	s_waitcnt vmcnt(12)
	s_cmp_eq_u64 s[4:5], 0
	s_cbranch_scc1 .Lhgc_e2_skip
	s_mov_b64 s[100:101], 0x1000
	v_add_u32_e32 v245, s26, v193
	v_add_u32_e32 v245, s25, v245
	v_add_u32_e32 v246, 0x7e, v245
	v_ashrrev_i32_e32 v247, 31, v246
	v_lshlrev_b64 v[182:183], 11, v[246:247]
	v_lshl_add_u64 v[182:183], v[130:131], 0, v[182:183]
	v_lshlrev_b64 v[184:185], 13, v[246:247]
	v_lshl_add_u64 v[184:185], v[132:133], 0, v[184:185]
	v_lshl_add_u64 v[184:185], v[184:185], 0, s[100:101]
	global_load_dword v197, v[182:183], off
	global_load_dword v198, v[182:183], off offset:64
	global_load_dword v199, v[182:183], off offset:128
	global_load_dword v200, v[182:183], off offset:192
	global_load_ushort v157, v[184:185], off offset:3072
	global_load_ushort v156, v[184:185], off offset:3104
	global_load_ushort v159, v[184:185], off offset:3136
	global_load_ushort v158, v[184:185], off offset:3168
	v_add_u32_e32 v246, 0x7d, v245
	v_ashrrev_i32_e32 v247, 31, v246
	v_lshlrev_b64 v[182:183], 11, v[246:247]
	v_lshl_add_u64 v[182:183], v[130:131], 0, v[182:183]
	v_lshlrev_b64 v[184:185], 13, v[246:247]
	v_lshl_add_u64 v[184:185], v[132:133], 0, v[184:185]
	v_lshl_add_u64 v[184:185], v[184:185], 0, s[100:101]
	global_load_dword v201, v[182:183], off
	global_load_dword v202, v[182:183], off offset:64
	global_load_dword v203, v[182:183], off offset:128
	global_load_dword v204, v[182:183], off offset:192
	global_load_ushort v161, v[184:185], off offset:3072
	global_load_ushort v160, v[184:185], off offset:3104
	global_load_ushort v162, v[184:185], off offset:3136
	global_load_ushort v163, v[184:185], off offset:3168
	v_add_u32_e32 v246, 0x7c, v245
	v_ashrrev_i32_e32 v247, 31, v246
	v_lshlrev_b64 v[182:183], 11, v[246:247]
	v_lshl_add_u64 v[182:183], v[130:131], 0, v[182:183]
	v_lshlrev_b64 v[184:185], 13, v[246:247]
	v_lshl_add_u64 v[184:185], v[132:133], 0, v[184:185]
	v_lshl_add_u64 v[184:185], v[184:185], 0, s[100:101]
	global_load_dword v205, v[182:183], off
	global_load_dword v206, v[182:183], off offset:64
	global_load_dword v209, v[182:183], off offset:128
	global_load_dword v212, v[182:183], off offset:192
	global_load_ushort v164, v[184:185], off offset:3072
	global_load_ushort v165, v[184:185], off offset:3104
	global_load_ushort v170, v[184:185], off offset:3136
	global_load_ushort v171, v[184:185], off offset:3168
	v_add_u32_e32 v246, 0x7f, v245
	v_ashrrev_i32_e32 v247, 31, v246
	v_lshlrev_b64 v[182:183], 11, v[246:247]
	v_lshl_add_u64 v[182:183], v[130:131], 0, v[182:183]
	v_lshlrev_b64 v[184:185], 13, v[246:247]
	v_lshl_add_u64 v[184:185], v[132:133], 0, v[184:185]
	v_lshl_add_u64 v[184:185], v[184:185], 0, s[100:101]
	global_load_dword v207, v[182:183], off
	global_load_dword v208, v[182:183], off offset:64
	global_load_dword v210, v[182:183], off offset:128
	global_load_dword v211, v[182:183], off offset:192
	global_load_ushort v167, v[184:185], off offset:3072
	global_load_ushort v166, v[184:185], off offset:3104
	global_load_ushort v169, v[184:185], off offset:3136
	global_load_ushort v168, v[184:185], off offset:3168
.Lhgc_e2_skip:
	v_sub_f32_e32 v93, 1.0, v80
	v_and_b32_e32 v90, 0xffff0000, v90
	v_mul_f32_e32 v90, 0xbfb8aa3b, v90
	v_add_f32_e32 v3, 1.0, v3
	v_rcp_f32_e32 v3, v3
	v_exp_f32_e32 v90, v90
	v_lshlrev_b32_e32 v92, 16, v91
	v_and_b32_e32 v91, 0xffff0000, v91
	v_fma_f32 v3, v3, v93, v80
	v_max_f32_e32 v3, 0xda24260, v3
	v_add_f32_e32 v90, 1.0, v90
	v_sub_f32_e32 v100, 1.0, v3
	v_log_f32_e32 v80, v3
	v_rcp_f32_e32 v90, v90
	v_mul_f32_e32 v91, 0xbfb8aa3b, v91
	v_exp_f32_e32 v91, v91
	v_mul_f32_e32 v3, 0x3f317217, v80
	v_fma_f32 v3, v80, s93, -v3
	v_fmac_f32_e32 v3, 0x3377d1cf, v80
	v_fmac_f32_e32 v3, 0x3f317217, v80
	v_add_f32_e32 v91, 1.0, v91
	v_rcp_f32_e32 v91, v91
	v_sub_f32_e32 v80, 1.0, v81
	v_fma_f32 v80, v90, v80, v81
	v_max_f32_e32 v80, 0xda24260, v80
	v_mul_f32_e32 v90, 0xbfb8aa3b, v92
	v_log_f32_e32 v81, v80
	v_exp_f32_e32 v90, v90
	v_sub_f32_e32 v101, 1.0, v80
	v_lshlrev_b32_e32 v92, 16, v88
	v_mul_f32_e32 v80, 0x3f317217, v81
	v_add_f32_e32 v90, 1.0, v90
	v_fma_f32 v80, v81, s93, -v80
	v_rcp_f32_e32 v90, v90
	v_fmac_f32_e32 v80, 0x3377d1cf, v81
	v_fmac_f32_e32 v80, 0x3f317217, v81
	v_mul_f32_e32 v92, 0xbfb8aa3b, v92
	v_exp_f32_e32 v92, v92
	v_sub_f32_e32 v81, 1.0, v82
	v_fma_f32 v81, v90, v81, v82
	v_max_f32_e32 v81, 0xda24260, v81
	v_cmp_gt_f32_e32 vcc, s92, v81
	v_add_f32_e32 v92, 1.0, v92
	v_rcp_f32_e32 v92, v92
	v_cndmask_b32_e64 v82, 0, 32, vcc
	v_ldexp_f32 v82, v81, v82
	v_log_f32_e32 v90, v82
	v_sub_f32_e32 v82, 1.0, v81
	v_mul_f32_e32 v81, 0x3f317217, v90
	v_fma_f32 v81, v90, s93, -v81
	v_fmac_f32_e32 v81, 0x3377d1cf, v90
	v_fmac_f32_e32 v81, 0x3f317217, v90
	v_cmp_lt_f32_e64 s[48:49], |v90|, s90
	v_and_b32_e32 v88, 0xffff0000, v88
	v_mul_f32_e32 v88, 0xbfb8aa3b, v88
	v_cndmask_b32_e64 v81, v90, v81, s[48:49]
	v_sub_f32_e32 v90, 1.0, v83
	v_fmac_f32_e32 v83, v91, v90
	v_max_f32_e32 v83, 0xda24260, v83
	v_cndmask_b32_e32 v91, 0, v179, vcc
	v_sub_f32_e32 v81, v81, v91
	v_log_f32_e32 v90, v83
	v_exp_f32_e32 v88, v88
	v_mov_b32_e32 v227, v3
	v_add_f32_dpp v3, v3, v3 row_shr:1 row_mask:0xf bank_mask:0xf bound_ctrl:1
	v_mul_f32_e32 v91, 0x3f317217, v90
	v_fma_f32 v91, v90, s93, -v91
	v_fmac_f32_e32 v91, 0x3377d1cf, v90
	v_fmac_f32_e32 v91, 0x3f317217, v90
	v_add_f32_e32 v88, 1.0, v88
	v_rcp_f32_e32 v88, v88
	v_mov_b32_e32 v90, v91
	v_sub_f32_e32 v91, 1.0, v76
	v_fma_f32 v76, v92, v91, v76
	v_max_f32_e32 v76, 0xda24260, v76
	v_sub_f32_e32 v102, 1.0, v76
	v_lshlrev_b32_e32 v92, 16, v89
	v_log_f32_e32 v91, v76
; #define LAS __attribute__((address_space(3)))
; __device__ __forceinline__ float sigmoidf_(float x) { return __builtin_amdgcn_rcpf(1.0f + __expf(-x)); }
; template <int CTRL> __device__ __forceinline__ float dpp_add0(float x) { return x + dppf<CTRL>(0.0f, x); }
; template <bool WITHO, bool RAW = false>
; __device__ __forceinline__ void hg_pass(const Frame& F, const bf16_t* P, const float* lbh, int b, int h, int nb, int dir, f32x4 (&S)[4][4], float (&Gsum)[16],
;                                         LAS bf16_t* Vl, LAS bf16_t* Kl, float* OF, const float* ngp) {
;     ...
;         for (int m = 0; m < 4; ++m) { const float z0 = __uint_as_float(zr[m].x << 16), z1 = __uint_as_float(zr[m].x & 0xffff0000u), z2 = __uint_as_float(zr[m].y << 16), z3 = __uint_as_float(zr[m].y & 0xffff0000u);
;             const float zz[4] = {z0, z1, z2, z3};
;             const f32x4 lb4 = *(const f32x4*)(lbh + 16 * m + 4 * g);
; #pragma unroll
;             for (int i = 0; i < 4; ++i) { const float lb = lb4[i]; const float f = fmaxf(lb + (1.0f - lb) * sigmoidf_(zz[i]), 1e-30f); kk[m * 4 + i] = 1.0f - f; c[m * 4 + i] = __logf(f); }
;             *(LAS u32x2*)(Vl + tau * 64 + 16 * m + 4 * g) = vr[m];
;  }
;         if (ci + 1 < HG_U / 16) { const int pos = (ci + 1) * 16 + tau, t = dir ? (HG_U - 1 - pos) : pos; const bf16_t* pr = P + (size_t)hg_row(b, nb, t) * 4096 + h * 64 + 4 * g;
; #pragma unroll
;             for (int m = 0; m < 4; ++m) { zr[m] = *(const u32x2*)(pr + (dir ? 2560 : 2048) + 16 * m); vr[m] = *(const u32x2*)(pr + 3072 + 16 * m); } }
;         float G[16];
; #pragma unroll
;         for (int q = 0; q < 16; ++q) G[q] = c[q];
; #pragma unroll
;         for (int q = 0; q < 16; q += 4) ROW_ALLREDUCE4(G[q], G[q + 1], G[q + 2], G[q + 3]);
; #pragma unroll
;         for (int q = 0; q < 16; ++q) { c[q] = dpp_add0<0x111>(c[q]); c[q] = dpp_add0<0x112>(c[q]); c[q] = dpp_add0<0x114>(c[q]); c[q] = dpp_add0<0x118>(c[q]); }
	v_and_b32_e32 v89, 0xffff0000, v89
	v_mul_f32_e32 v89, 0xbfb8aa3b, v89
	v_exp_f32_e32 v89, v89
	v_mul_f32_e32 v76, 0x3f317217, v91
	v_fma_f32 v76, v91, s93, -v76
	v_fmac_f32_e32 v76, 0x3377d1cf, v91
	v_fmac_f32_e32 v76, 0x3f317217, v91
	v_add_f32_e32 v89, 1.0, v89
	v_rcp_f32_e32 v89, v89
	v_sub_f32_e32 v91, 1.0, v77
	v_fma_f32 v77, v88, v91, v77
	v_max_f32_e32 v77, 0xda24260, v77
	v_mul_f32_e32 v91, 0xbfb8aa3b, v92
	v_log_f32_e32 v88, v77
	v_exp_f32_e32 v91, v91
	v_sub_f32_e32 v103, 1.0, v77
	v_lshlrev_b32_e32 v92, 16, v84
	v_mul_f32_e32 v77, 0x3f317217, v88
	v_add_f32_e32 v91, 1.0, v91
	v_fma_f32 v77, v88, s93, -v77
	v_rcp_f32_e32 v91, v91
	v_fmac_f32_e32 v77, 0x3377d1cf, v88
	v_fmac_f32_e32 v77, 0x3f317217, v88
	v_mul_f32_e32 v92, 0xbfb8aa3b, v92
	v_exp_f32_e32 v92, v92
	v_sub_f32_e32 v88, 1.0, v78
	v_fma_f32 v78, v91, v88, v78
	v_max_f32_e32 v78, 0xda24260, v78
	v_sub_f32_e32 v104, 1.0, v78
	v_log_f32_e32 v88, v78
	v_lshlrev_b32_e32 v91, 16, v87
	v_mul_f32_e32 v91, 0xbfb8aa3b, v91
	v_mul_f32_e32 v78, 0x3f317217, v88
	v_fma_f32 v78, v88, s93, -v78
	v_fmac_f32_e32 v78, 0x3377d1cf, v88
	v_fmac_f32_e32 v78, 0x3f317217, v88
	v_exp_f32_e32 v91, v91
	v_and_b32_e32 v87, 0xffff0000, v87
	v_sub_f32_e32 v88, 1.0, v79
	v_fmac_f32_e32 v79, v89, v88
	v_max_f32_e32 v79, 0xda24260, v79
	v_sub_f32_e32 v105, 1.0, v79
	v_mov_b32_e32 v88, v79
	v_lshlrev_b32_e32 v79, 16, v86
	v_log_f32_e32 v88, v88
	v_mul_f32_e32 v79, 0xbfb8aa3b, v79
	v_exp_f32_e32 v79, v79
	v_mov_b32_e32 v89, v78
	v_mul_f32_e32 v78, 0x3f317217, v88
	v_fma_f32 v78, v88, s93, -v78
	v_add_f32_e32 v79, 1.0, v79
	v_fmac_f32_e32 v78, 0x3377d1cf, v88
	v_rcp_f32_e32 v79, v79
	v_fmac_f32_e32 v78, 0x3f317217, v88
	v_and_b32_e32 v86, 0xffff0000, v86
	v_mul_f32_e32 v86, 0xbfb8aa3b, v86
	v_mov_b32_e32 v88, v78
	v_sub_f32_e32 v78, 1.0, v72
	v_fma_f32 v72, v79, v78, v72
	v_max_f32_e32 v72, 0xda24260, v72
	v_cmp_gt_f32_e32 vcc, s92, v72
	v_exp_f32_e32 v86, v86
	v_add_f32_e32 v91, 1.0, v91
	v_cndmask_b32_e64 v78, 0, 32, vcc
	v_ldexp_f32 v78, v72, v78
	v_log_f32_e32 v79, v78
	v_sub_f32_e32 v78, 1.0, v72
	v_add_f32_e32 v86, 1.0, v86
	v_rcp_f32_e32 v86, v86
	v_mul_f32_e32 v72, 0x3f317217, v79
	v_fma_f32 v72, v79, s93, -v72
	v_fmac_f32_e32 v72, 0x3377d1cf, v79
	v_fmac_f32_e32 v72, 0x3f317217, v79
	v_cmp_lt_f32_e64 s[48:49], |v79|, s90
	v_rcp_f32_e32 v91, v91
	v_mul_f32_e32 v87, 0xbfb8aa3b, v87
	v_cndmask_b32_e64 v72, v79, v72, s[48:49]
	v_sub_f32_e32 v79, 1.0, v73
	v_fma_f32 v73, v86, v79, v73
	v_max_f32_e32 v73, 0xda24260, v73
	v_cmp_gt_f32_e64 s[48:49], s92, v73
	v_exp_f32_e32 v87, v87
	v_add_f32_e32 v92, 1.0, v92
	v_cndmask_b32_e64 v79, 0, 32, s[48:49]
	v_ldexp_f32 v79, v73, v79
	v_log_f32_e32 v86, v79
	v_cndmask_b32_e32 v79, 0, v179, vcc
	v_sub_f32_e32 v72, v72, v79
	v_sub_f32_e32 v79, 1.0, v73
	v_mul_f32_e32 v73, 0x3f317217, v86
	v_fma_f32 v73, v86, s93, -v73
	v_fmac_f32_e32 v73, 0x3377d1cf, v86
	v_fmac_f32_e32 v73, 0x3f317217, v86
	v_cmp_lt_f32_e64 vcc, |v86|, s90
	v_add_f32_e32 v87, 1.0, v87
	v_rcp_f32_e32 v87, v87
	v_cndmask_b32_e32 v73, v86, v73, vcc
	v_sub_f32_e32 v86, 1.0, v74
	v_fma_f32 v74, v91, v86, v74
	v_max_f32_e32 v74, 0xda24260, v74
	v_cndmask_b32_e64 v91, 0, v179, s[48:49]
	v_sub_f32_e32 v73, v73, v91
	v_log_f32_e32 v86, v74
	v_rcp_f32_e32 v92, v92
	v_and_b32_e32 v84, 0xffff0000, v84
	v_mul_f32_e32 v84, 0xbfb8aa3b, v84
	v_mul_f32_e32 v91, 0x3f317217, v86
	v_fma_f32 v91, v86, s93, -v91
	v_fmac_f32_e32 v91, 0x3377d1cf, v86
	v_fmac_f32_e32 v91, 0x3f317217, v86
	v_exp_f32_e32 v84, v84
	v_add_f32_dpp v3, v3, v3 row_shr:2 row_mask:0xf bank_mask:0xf bound_ctrl:1
	v_mov_b32_e32 v86, v91
	v_sub_f32_e32 v91, 1.0, v75
	v_fmac_f32_e32 v75, v87, v91
	v_max_f32_e32 v75, 0xda24260, v75
	v_log_f32_e32 v87, v75
	v_add_f32_e32 v84, 1.0, v84
	v_rcp_f32_e32 v84, v84
	v_add_f32_dpp v3, v3, v3 row_shr:4 row_mask:0xf bank_mask:0xf bound_ctrl:1
	v_mul_f32_e32 v91, 0x3f317217, v87
	v_fma_f32 v91, v87, s93, -v91
	v_fmac_f32_e32 v91, 0x3377d1cf, v87
	v_fmac_f32_e32 v91, 0x3f317217, v87
	v_add_f32_dpp v244, v3, v3 row_shr:8 row_mask:0xf bank_mask:0xf bound_ctrl:1
	v_add_f32_dpp v3, v80, v80 row_shr:1 row_mask:0xf bank_mask:0xf bound_ctrl:1
	v_mov_b32_e32 v87, v91
	v_sub_f32_e32 v91, 1.0, v68
	v_fma_f32 v68, v92, v91, v68
	v_max_f32_e32 v68, 0xda24260, v68
	v_sub_f32_e32 v229, 1.0, v68
	v_add_f32_dpp v3, v3, v3 row_shr:2 row_mask:0xf bank_mask:0xf bound_ctrl:1
	v_log_f32_e32 v91, v68
	v_lshlrev_b32_e32 v92, 16, v85
	v_add_f32_dpp v3, v3, v3 row_shr:4 row_mask:0xf bank_mask:0xf bound_ctrl:1
	v_and_b32_e32 v85, 0xffff0000, v85
	v_mul_f32_e32 v68, 0x3f317217, v91
	v_fma_f32 v68, v91, s93, -v68
	v_fmac_f32_e32 v68, 0x3377d1cf, v91
	v_fmac_f32_e32 v68, 0x3f317217, v91
	v_add_f32_dpp v243, v3, v3 row_shr:8 row_mask:0xf bank_mask:0xf bound_ctrl:1
	v_add_f32_dpp v3, v81, v81 row_shr:1 row_mask:0xf bank_mask:0xf bound_ctrl:1
	v_sub_f32_e32 v91, 1.0, v69
	v_fma_f32 v69, v84, v91, v69
	v_max_f32_e32 v69, 0xda24260, v69
	v_mul_f32_e32 v91, 0xbfb8aa3b, v92
	v_log_f32_e32 v84, v69
	v_exp_f32_e32 v91, v91
	v_add_f32_dpp v3, v3, v3 row_shr:2 row_mask:0xf bank_mask:0xf bound_ctrl:1
	v_sub_f32_e32 v230, 1.0, v69
	v_mul_f32_e32 v69, 0x3f317217, v84
	v_add_f32_dpp v3, v3, v3 row_shr:4 row_mask:0xf bank_mask:0xf bound_ctrl:1
	v_add_f32_e32 v91, 1.0, v91
	v_fma_f32 v69, v84, s93, -v69
	v_add_f32_dpp v242, v3, v3 row_shr:8 row_mask:0xf bank_mask:0xf bound_ctrl:1
	v_add_f32_dpp v3, v90, v90 row_shr:1 row_mask:0xf bank_mask:0xf bound_ctrl:1
	v_rcp_f32_e32 v91, v91
	v_fmac_f32_e32 v69, 0x3377d1cf, v84
	v_add_f32_dpp v3, v3, v3 row_shr:2 row_mask:0xf bank_mask:0xf bound_ctrl:1
	v_fmac_f32_e32 v69, 0x3f317217, v84
	s_nop 0
; template <int CTRL> __device__ __forceinline__ float dpp_add0(float x) { return x + dppf<CTRL>(0.0f, x); }
; template <bool WITHO, bool RAW = false>
; __device__ __forceinline__ void hg_pass(const Frame& F, const bf16_t* P, const float* lbh, int b, int h, int nb, int dir, f32x4 (&S)[4][4], float (&Gsum)[16],
;                                         LAS bf16_t* Vl, LAS bf16_t* Kl, float* OF, const float* ngp) {
;     ...
;         for (int q = 0; q < 16; ++q) G[q] = c[q];
; #pragma unroll
;         for (int q = 0; q < 16; q += 4) ROW_ALLREDUCE4(G[q], G[q + 1], G[q + 2], G[q + 3]);
; #pragma unroll
;         for (int q = 0; q < 16; ++q) { c[q] = dpp_add0<0x111>(c[q]); c[q] = dpp_add0<0x112>(c[q]); c[q] = dpp_add0<0x114>(c[q]); c[q] = dpp_add0<0x118>(c[q]); }
; #pragma unroll
;         for (int q = 0; q < 16; ++q) Gsum[q] += G[q];
; #pragma unroll
;         for (int m = 0; m < 4; ++m) { float kh[4];
; #pragma unroll
;             for (int i = 0; i < 4; ++i) kh[i] = kk[m * 4 + i] * __expf(G[m * 4 + i] - c[m * 4 + i]);
	v_add_f32_dpp v3, v3, v3 row_shr:4 row_mask:0xf bank_mask:0xf bound_ctrl:1
	v_mul_f32_e32 v85, 0xbfb8aa3b, v85
	s_nop 0
	v_add_f32_dpp v241, v3, v3 row_shr:8 row_mask:0xf bank_mask:0xf bound_ctrl:1
	v_add_f32_dpp v3, v76, v76 row_shr:1 row_mask:0xf bank_mask:0xf bound_ctrl:1
	v_sub_f32_e32 v84, 1.0, v70
	v_fma_f32 v70, v91, v84, v70
	v_add_f32_dpp v3, v3, v3 row_shr:2 row_mask:0xf bank_mask:0xf bound_ctrl:1
	v_max_f32_e32 v70, 0xda24260, v70
	s_nop 0
	v_add_f32_dpp v3, v3, v3 row_shr:4 row_mask:0xf bank_mask:0xf bound_ctrl:1
	v_exp_f32_e32 v85, v85
	s_nop 0
	v_add_f32_dpp v109, v3, v3 row_shr:8 row_mask:0xf bank_mask:0xf bound_ctrl:1
	v_add_f32_dpp v3, v77, v77 row_shr:1 row_mask:0xf bank_mask:0xf bound_ctrl:1
	v_log_f32_e32 v84, v70
	s_nop 0
	v_add_f32_dpp v3, v3, v3 row_shr:2 row_mask:0xf bank_mask:0xf bound_ctrl:1
	v_sub_f32_e32 v231, 1.0, v70
	v_add_f32_e32 v85, 1.0, v85
	v_add_f32_dpp v3, v3, v3 row_shr:4 row_mask:0xf bank_mask:0xf bound_ctrl:1
	v_mul_f32_e32 v70, 0x3f317217, v84
	v_fma_f32 v70, v84, s93, -v70
	v_add_f32_dpp v108, v3, v3 row_shr:8 row_mask:0xf bank_mask:0xf bound_ctrl:1
	v_add_f32_dpp v3, v89, v89 row_shr:1 row_mask:0xf bank_mask:0xf bound_ctrl:1
	v_rcp_f32_e32 v85, v85
	v_fmac_f32_e32 v70, 0x3377d1cf, v84
	v_add_f32_dpp v3, v3, v3 row_shr:2 row_mask:0xf bank_mask:0xf bound_ctrl:1
	v_fmac_f32_e32 v70, 0x3f317217, v84
	s_nop 0
	v_add_f32_dpp v3, v3, v3 row_shr:4 row_mask:0xf bank_mask:0xf bound_ctrl:1
	s_nop 1
	v_add_f32_dpp v107, v3, v3 row_shr:8 row_mask:0xf bank_mask:0xf bound_ctrl:1
	v_add_f32_dpp v3, v88, v88 row_shr:1 row_mask:0xf bank_mask:0xf bound_ctrl:1
	v_sub_f32_e32 v84, 1.0, v71
	s_nop 0
	v_add_f32_dpp v3, v3, v3 row_shr:2 row_mask:0xf bank_mask:0xf bound_ctrl:1
	v_fmac_f32_e32 v71, v85, v84
	v_max_f32_e32 v71, 0xda24260, v71
	v_add_f32_dpp v3, v3, v3 row_shr:4 row_mask:0xf bank_mask:0xf bound_ctrl:1
	v_sub_f32_e32 v232, 1.0, v71
	s_nop 0
	v_add_f32_dpp v106, v3, v3 row_shr:8 row_mask:0xf bank_mask:0xf bound_ctrl:1
	v_add_f32_dpp v3, v72, v72 row_shr:1 row_mask:0xf bank_mask:0xf bound_ctrl:1
	s_nop 1
	v_add_f32_dpp v3, v3, v3 row_shr:2 row_mask:0xf bank_mask:0xf bound_ctrl:1
	v_log_f32_e32 v84, v71
	s_nop 0
	v_add_f32_dpp v3, v3, v3 row_shr:4 row_mask:0xf bank_mask:0xf bound_ctrl:1
	v_mul_f32_e32 v71, 0x3f317217, v84
	s_nop 0
	v_add_f32_dpp v240, v3, v3 row_shr:8 row_mask:0xf bank_mask:0xf bound_ctrl:1
	v_add_f32_dpp v3, v73, v73 row_shr:1 row_mask:0xf bank_mask:0xf bound_ctrl:1
	v_fma_f32 v71, v84, s93, -v71
	v_fmac_f32_e32 v71, 0x3377d1cf, v84
	v_add_f32_dpp v3, v3, v3 row_shr:2 row_mask:0xf bank_mask:0xf bound_ctrl:1
	v_fmac_f32_e32 v71, 0x3f317217, v84
	s_nop 0
	v_add_f32_dpp v3, v3, v3 row_shr:4 row_mask:0xf bank_mask:0xf bound_ctrl:1
	v_mov_b32_e32 v225, v90
	s_nop 0
	v_add_f32_dpp v239, v3, v3 row_shr:8 row_mask:0xf bank_mask:0xf bound_ctrl:1
	v_add_f32_dpp v3, v86, v86 row_shr:1 row_mask:0xf bank_mask:0xf bound_ctrl:1
	s_nop 1
	v_add_f32_dpp v3, v3, v3 row_shr:2 row_mask:0xf bank_mask:0xf bound_ctrl:1
	v_mov_b32_e32 v226, v81
	v_mov_b32_e32 v228, v80
	v_add_f32_dpp v3, v3, v3 row_shr:4 row_mask:0xf bank_mask:0xf bound_ctrl:1
	s_nop 1
	v_add_f32_dpp v227, v227, v227 quad_perm:[1,0,3,2] row_mask:0xf bank_mask:0xf
	v_add_f32_dpp v228, v228, v228 quad_perm:[1,0,3,2] row_mask:0xf bank_mask:0xf
	v_add_f32_dpp v226, v226, v226 quad_perm:[1,0,3,2] row_mask:0xf bank_mask:0xf
	v_add_f32_dpp v225, v225, v225 quad_perm:[1,0,3,2] row_mask:0xf bank_mask:0xf
	v_add_f32_dpp v227, v227, v227 quad_perm:[2,3,0,1] row_mask:0xf bank_mask:0xf
	v_add_f32_dpp v228, v228, v228 quad_perm:[2,3,0,1] row_mask:0xf bank_mask:0xf
	v_add_f32_dpp v226, v226, v226 quad_perm:[2,3,0,1] row_mask:0xf bank_mask:0xf
	v_add_f32_dpp v225, v225, v225 quad_perm:[2,3,0,1] row_mask:0xf bank_mask:0xf
	v_add_f32_dpp v227, v227, v227 row_half_mirror row_mask:0xf bank_mask:0xf
	v_add_f32_dpp v228, v228, v228 row_half_mirror row_mask:0xf bank_mask:0xf
	v_add_f32_dpp v226, v226, v226 row_half_mirror row_mask:0xf bank_mask:0xf
	v_add_f32_dpp v225, v225, v225 row_half_mirror row_mask:0xf bank_mask:0xf
	v_add_f32_dpp v227, v227, v227 row_mirror row_mask:0xf bank_mask:0xf
	v_add_f32_dpp v228, v228, v228 row_mirror row_mask:0xf bank_mask:0xf
	v_add_f32_dpp v226, v226, v226 row_mirror row_mask:0xf bank_mask:0xf
	v_add_f32_dpp v225, v225, v225 row_mirror row_mask:0xf bank_mask:0xf
	v_mov_b32_e32 v215, v68
	v_mov_b32_e32 v216, v69
	v_add_f32_dpp v238, v3, v3 row_shr:8 row_mask:0xf bank_mask:0xf bound_ctrl:1
	v_add_f32_dpp v3, v87, v87 row_shr:1 row_mask:0xf bank_mask:0xf bound_ctrl:1
	v_mov_b32_e32 v213, v70
	v_mov_b32_e32 v221, v89
	v_add_f32_dpp v3, v3, v3 row_shr:2 row_mask:0xf bank_mask:0xf bound_ctrl:1
	v_mov_b32_e32 v223, v77
	v_mov_b32_e32 v222, v88
	v_add_f32_dpp v3, v3, v3 row_shr:4 row_mask:0xf bank_mask:0xf bound_ctrl:1
	v_mov_b32_e32 v224, v76
	v_mov_b32_e32 v218, v73
	v_add_f32_dpp v237, v3, v3 row_shr:8 row_mask:0xf bank_mask:0xf bound_ctrl:1
	v_add_f32_dpp v3, v68, v68 row_shr:1 row_mask:0xf bank_mask:0xf bound_ctrl:1
	v_sub_f32_e32 v68, v228, v243
	v_mul_f32_e32 v68, 0x3fb8aa3b, v68
	v_add_f32_dpp v3, v3, v3 row_shr:2 row_mask:0xf bank_mask:0xf bound_ctrl:1
	v_exp_f32_e32 v68, v68
	v_mov_b32_e32 v217, v87
	v_add_f32_dpp v3, v3, v3 row_shr:4 row_mask:0xf bank_mask:0xf bound_ctrl:1
	v_mov_b32_e32 v220, v72
	v_mov_b32_e32 v219, v86
	v_add_f32_dpp v236, v3, v3 row_shr:8 row_mask:0xf bank_mask:0xf bound_ctrl:1
	v_add_f32_dpp v3, v69, v69 row_shr:1 row_mask:0xf bank_mask:0xf bound_ctrl:1
	v_sub_f32_e32 v69, v226, v242
	v_mul_f32_e32 v69, 0x3fb8aa3b, v69
	v_add_f32_dpp v3, v3, v3 row_shr:2 row_mask:0xf bank_mask:0xf bound_ctrl:1
	v_exp_f32_e32 v69, v69
; template <int CTRL> __device__ __forceinline__ float dpp_add0(float x) { return x + dppf<CTRL>(0.0f, x); }
; template <bool WITHO, bool RAW = false>
; __device__ __forceinline__ void hg_pass(const Frame& F, const bf16_t* P, const float* lbh, int b, int h, int nb, int dir, f32x4 (&S)[4][4], float (&Gsum)[16],
;                                         LAS bf16_t* Vl, LAS bf16_t* Kl, float* OF, const float* ngp) {
;     ...
;         for (int q = 0; q < 16; ++q) G[q] = c[q];
; #pragma unroll
;         for (int q = 0; q < 16; q += 4) ROW_ALLREDUCE4(G[q], G[q + 1], G[q + 2], G[q + 3]);
; #pragma unroll
;         for (int q = 0; q < 16; ++q) { c[q] = dpp_add0<0x111>(c[q]); c[q] = dpp_add0<0x112>(c[q]); c[q] = dpp_add0<0x114>(c[q]); c[q] = dpp_add0<0x118>(c[q]); }
; #pragma unroll
;         for (int q = 0; q < 16; ++q) Gsum[q] += G[q];
; #pragma unroll
;         for (int m = 0; m < 4; ++m) { float kh[4];
; #pragma unroll
;             for (int i = 0; i < 4; ++i) kh[i] = kk[m * 4 + i] * __expf(G[m * 4 + i] - c[m * 4 + i]);
	v_mov_b32_e32 v214, v71
	v_add_f32_dpp v3, v3, v3 row_shr:4 row_mask:0xf bank_mask:0xf bound_ctrl:1
	v_mul_f32_e32 v68, v101, v68
	v_sub_f32_e32 v83, 1.0, v83
	v_add_f32_dpp v235, v3, v3 row_shr:8 row_mask:0xf bank_mask:0xf bound_ctrl:1
	v_add_f32_dpp v3, v70, v70 row_shr:1 row_mask:0xf bank_mask:0xf bound_ctrl:1
	v_sub_f32_e32 v70, v225, v241
	v_mul_f32_e32 v70, 0x3fb8aa3b, v70
	v_add_f32_dpp v3, v3, v3 row_shr:2 row_mask:0xf bank_mask:0xf bound_ctrl:1
	v_exp_f32_e32 v70, v70
	s_nop 1
	v_add_f32_dpp v224, v224, v224 quad_perm:[1,0,3,2] row_mask:0xf bank_mask:0xf
	v_add_f32_dpp v223, v223, v223 quad_perm:[1,0,3,2] row_mask:0xf bank_mask:0xf
	v_add_f32_dpp v221, v221, v221 quad_perm:[1,0,3,2] row_mask:0xf bank_mask:0xf
	v_add_f32_dpp v222, v222, v222 quad_perm:[1,0,3,2] row_mask:0xf bank_mask:0xf
	v_add_f32_dpp v224, v224, v224 quad_perm:[2,3,0,1] row_mask:0xf bank_mask:0xf
	v_add_f32_dpp v223, v223, v223 quad_perm:[2,3,0,1] row_mask:0xf bank_mask:0xf
	v_add_f32_dpp v221, v221, v221 quad_perm:[2,3,0,1] row_mask:0xf bank_mask:0xf
	v_add_f32_dpp v222, v222, v222 quad_perm:[2,3,0,1] row_mask:0xf bank_mask:0xf
	v_add_f32_dpp v224, v224, v224 row_half_mirror row_mask:0xf bank_mask:0xf
	v_add_f32_dpp v223, v223, v223 row_half_mirror row_mask:0xf bank_mask:0xf
	v_add_f32_dpp v221, v221, v221 row_half_mirror row_mask:0xf bank_mask:0xf
	v_add_f32_dpp v222, v222, v222 row_half_mirror row_mask:0xf bank_mask:0xf
	v_add_f32_dpp v224, v224, v224 row_mirror row_mask:0xf bank_mask:0xf
	v_add_f32_dpp v223, v223, v223 row_mirror row_mask:0xf bank_mask:0xf
	v_add_f32_dpp v221, v221, v221 row_mirror row_mask:0xf bank_mask:0xf
	v_add_f32_dpp v222, v222, v222 row_mirror row_mask:0xf bank_mask:0xf
	s_nop 1
	v_add_f32_dpp v220, v220, v220 quad_perm:[1,0,3,2] row_mask:0xf bank_mask:0xf
	v_add_f32_dpp v218, v218, v218 quad_perm:[1,0,3,2] row_mask:0xf bank_mask:0xf
	v_add_f32_dpp v219, v219, v219 quad_perm:[1,0,3,2] row_mask:0xf bank_mask:0xf
	v_add_f32_dpp v217, v217, v217 quad_perm:[1,0,3,2] row_mask:0xf bank_mask:0xf
	v_add_f32_dpp v220, v220, v220 quad_perm:[2,3,0,1] row_mask:0xf bank_mask:0xf
	v_add_f32_dpp v218, v218, v218 quad_perm:[2,3,0,1] row_mask:0xf bank_mask:0xf
	v_add_f32_dpp v219, v219, v219 quad_perm:[2,3,0,1] row_mask:0xf bank_mask:0xf
	v_add_f32_dpp v217, v217, v217 quad_perm:[2,3,0,1] row_mask:0xf bank_mask:0xf
	v_add_f32_dpp v220, v220, v220 row_half_mirror row_mask:0xf bank_mask:0xf
	v_add_f32_dpp v218, v218, v218 row_half_mirror row_mask:0xf bank_mask:0xf
	v_add_f32_dpp v219, v219, v219 row_half_mirror row_mask:0xf bank_mask:0xf
	v_add_f32_dpp v217, v217, v217 row_half_mirror row_mask:0xf bank_mask:0xf
	v_add_f32_dpp v220, v220, v220 row_mirror row_mask:0xf bank_mask:0xf
	v_add_f32_dpp v218, v218, v218 row_mirror row_mask:0xf bank_mask:0xf
	v_add_f32_dpp v219, v219, v219 row_mirror row_mask:0xf bank_mask:0xf
	v_add_f32_dpp v217, v217, v217 row_mirror row_mask:0xf bank_mask:0xf
	s_nop 1
	v_add_f32_dpp v215, v215, v215 quad_perm:[1,0,3,2] row_mask:0xf bank_mask:0xf
	v_add_f32_dpp v216, v216, v216 quad_perm:[1,0,3,2] row_mask:0xf bank_mask:0xf
	v_add_f32_dpp v213, v213, v213 quad_perm:[1,0,3,2] row_mask:0xf bank_mask:0xf
	v_add_f32_dpp v214, v214, v214 quad_perm:[1,0,3,2] row_mask:0xf bank_mask:0xf
	v_add_f32_dpp v215, v215, v215 quad_perm:[2,3,0,1] row_mask:0xf bank_mask:0xf
	v_add_f32_dpp v216, v216, v216 quad_perm:[2,3,0,1] row_mask:0xf bank_mask:0xf
	v_add_f32_dpp v213, v213, v213 quad_perm:[2,3,0,1] row_mask:0xf bank_mask:0xf
	v_add_f32_dpp v214, v214, v214 quad_perm:[2,3,0,1] row_mask:0xf bank_mask:0xf
	v_add_f32_dpp v215, v215, v215 row_half_mirror row_mask:0xf bank_mask:0xf
	v_add_f32_dpp v216, v216, v216 row_half_mirror row_mask:0xf bank_mask:0xf
	v_add_f32_dpp v213, v213, v213 row_half_mirror row_mask:0xf bank_mask:0xf
	v_add_f32_dpp v214, v214, v214 row_half_mirror row_mask:0xf bank_mask:0xf
	v_add_f32_dpp v215, v215, v215 row_mirror row_mask:0xf bank_mask:0xf
	v_add_f32_dpp v216, v216, v216 row_mirror row_mask:0xf bank_mask:0xf
; #define LAS __attribute__((address_space(3)))
; __device__ __forceinline__ float bf2f(unsigned short b) { return __uint_as_float(((unsigned)b) << 16); }
; __device__ __forceinline__ unsigned cvt_pk_bf16(float lo, float hi) { unsigned r; asm volatile("v_cvt_pk_bf16_f32 %0, %1, %2" : "=v"(r) : "v"(lo), "v"(hi)); return r; }
; template <bool WITHO, bool RAW = false>
; __device__ __forceinline__ void hg_pass(const Frame& F, const bf16_t* P, const float* lbh, int b, int h, int nb, int dir, f32x4 (&S)[4][4], float (&Gsum)[16],
;                                         LAS bf16_t* Vl, LAS bf16_t* Kl, float* OF, const float* ngp) {
;     ...
;         for (int q = 0; q < 16; ++q) Gsum[q] += G[q];
; #pragma unroll
;         for (int m = 0; m < 4; ++m) { float kh[4];
; #pragma unroll
;             for (int i = 0; i < 4; ++i) kh[i] = kk[m * 4 + i] * __expf(G[m * 4 + i] - c[m * 4 + i]);
;             u32x2 w; w.x = cvt_pk_bf16(kh[0], kh[1]); w.y = cvt_pk_bf16(kh[2], kh[3]);
;             *(LAS u32x2*)(Kl + tau * 64 + 16 * m + 4 * g) = w; }
;         float ofv[4][4], gtv[4][4]; int orow[4];
;         if (WITHO) {
; #pragma unroll
;             for (int i = 0; i < 4; ++i) { const int p2 = ci * 16 + 4 * g + i, t2 = dir ? (HG_U - 1 - p2) : p2; orow[i] = hg_row(b, nb, t2); }
;             if (dir && !RAW) {
; #pragma unroll
;                 for (int i = 0; i < 4; ++i)
; #pragma unroll
;                     for (int vt = 0; vt < 4; ++vt) { ofv[i][vt] = OF[(size_t)orow[i] * 512 + h * 64 + 16 * vt + tau]; gtv[i][vt] = bf2f(P[(size_t)orow[i] * 4096 + 3584 + h * 64 + 16 * vt + tau]); }
	v_add_f32_dpp v213, v213, v213 row_mirror row_mask:0xf bank_mask:0xf
	v_add_f32_dpp v214, v214, v214 row_mirror row_mask:0xf bank_mask:0xf
	v_mul_f32_e32 v69, v82, v69
	v_add_f32_dpp v3, v3, v3 row_shr:4 row_mask:0xf bank_mask:0xf bound_ctrl:1
	v_mul_f32_e32 v70, v83, v70
	v_sub_f32_e32 v74, 1.0, v74
	v_add_f32_dpp v234, v3, v3 row_shr:8 row_mask:0xf bank_mask:0xf bound_ctrl:1
	v_add_f32_dpp v3, v71, v71 row_shr:1 row_mask:0xf bank_mask:0xf bound_ctrl:1
	v_sub_f32_e32 v75, 1.0, v75
	s_andn2_b64 vcc, exec, s[4:5]
	v_add_f32_dpp v3, v3, v3 row_shr:2 row_mask:0xf bank_mask:0xf bound_ctrl:1
	s_nop 1
	v_add_f32_dpp v3, v3, v3 row_shr:4 row_mask:0xf bank_mask:0xf bound_ctrl:1
	s_nop 1
	v_add_f32_dpp v233, v3, v3 row_shr:8 row_mask:0xf bank_mask:0xf bound_ctrl:1
	v_sub_f32_e32 v3, v227, v244
	v_mul_f32_e32 v3, 0x3fb8aa3b, v3
	v_exp_f32_e32 v3, v3
	s_nop 0
	v_mul_f32_e32 v3, v100, v3
	v_cvt_pk_bf16_f32 v68, v3, v68
	v_cvt_pk_bf16_f32 v69, v69, v70
	ds_write_b64 v191, v[68:69] offset:34816
	v_sub_f32_e32 v68, v223, v108
	v_sub_f32_e32 v3, v224, v109
	v_mul_f32_e32 v68, 0x3fb8aa3b, v68
	v_sub_f32_e32 v69, v221, v107
	v_mul_f32_e32 v3, 0x3fb8aa3b, v3
	v_exp_f32_e32 v68, v68
	v_mul_f32_e32 v69, 0x3fb8aa3b, v69
	v_sub_f32_e32 v70, v222, v106
	v_exp_f32_e32 v3, v3
	v_exp_f32_e32 v69, v69
	v_mul_f32_e32 v70, 0x3fb8aa3b, v70
	v_exp_f32_e32 v70, v70
	v_mul_f32_e32 v68, v103, v68
	v_mul_f32_e32 v3, v102, v3
	v_mul_f32_e32 v69, v104, v69
	v_cvt_pk_bf16_f32 v68, v3, v68
	v_mul_f32_e32 v70, v105, v70
	v_cvt_pk_bf16_f32 v69, v69, v70
	ds_write_b64 v191, v[68:69] offset:34848
	v_sub_f32_e32 v68, v218, v239
	v_sub_f32_e32 v3, v220, v240
	v_mul_f32_e32 v68, 0x3fb8aa3b, v68
	v_sub_f32_e32 v69, v219, v238
	v_mul_f32_e32 v3, 0x3fb8aa3b, v3
	v_exp_f32_e32 v68, v68
	v_mul_f32_e32 v69, 0x3fb8aa3b, v69
	v_sub_f32_e32 v70, v217, v237
	v_exp_f32_e32 v3, v3
	v_exp_f32_e32 v69, v69
	v_mul_f32_e32 v70, 0x3fb8aa3b, v70
	v_exp_f32_e32 v70, v70
	v_mul_f32_e32 v68, v79, v68
	v_mul_f32_e32 v3, v78, v3
	v_mul_f32_e32 v69, v74, v69
	v_cvt_pk_bf16_f32 v68, v3, v68
	v_mul_f32_e32 v70, v75, v70
	v_cvt_pk_bf16_f32 v69, v69, v70
	ds_write_b64 v191, v[68:69] offset:34880
	v_sub_f32_e32 v68, v216, v235
	v_sub_f32_e32 v3, v215, v236
	v_mul_f32_e32 v68, 0x3fb8aa3b, v68
	v_sub_f32_e32 v69, v213, v234
	v_mul_f32_e32 v3, 0x3fb8aa3b, v3
	v_exp_f32_e32 v68, v68
	v_mul_f32_e32 v69, 0x3fb8aa3b, v69
	v_sub_f32_e32 v70, v214, v233
	v_exp_f32_e32 v3, v3
	v_exp_f32_e32 v69, v69
	v_mul_f32_e32 v70, 0x3fb8aa3b, v70
	v_exp_f32_e32 v70, v70
	v_mul_f32_e32 v68, v230, v68
	v_mul_f32_e32 v3, v229, v3
	v_mul_f32_e32 v69, v231, v69
	v_cvt_pk_bf16_f32 v68, v3, v68
	v_mul_f32_e32 v70, v232, v70
	v_cvt_pk_bf16_f32 v69, v69, v70
	ds_write_b64 v191, v[68:69] offset:34912
	v_add_u32_e32 v68, s26, v193
	v_add_u32_e32 v3, s27, v114
	v_add_u32_e32 v69, 0x7f, v68
	v_cndmask_b32_e64 v69, v69, v3, s[0:1]
	v_add_u32_e32 v172, s25, v69
	v_add_u32_e32 v69, 1, v3
	v_add_u32_e32 v70, 0x7e, v68
	v_cndmask_b32_e64 v69, v70, v69, s[0:1]
	v_add_u32_e32 v90, s25, v69
	v_add_u32_e32 v69, 2, v3
	v_add_u32_e32 v70, 0x7d, v68
	v_add_u32_e32 v3, 3, v3
	v_add_u32_e32 v68, 0x7c, v68
	v_cndmask_b32_e64 v69, v70, v69, s[0:1]
	v_cndmask_b32_e64 v3, v68, v3, s[0:1]
	v_add_u32_e32 v86, s25, v69
	v_add_u32_e32 v70, s25, v3
	v_ashrrev_i32_e32 v173, 31, v172
	v_ashrrev_i32_e32 v91, 31, v90
	v_ashrrev_i32_e32 v87, 31, v86
	v_ashrrev_i32_e32 v71, 31, v70
	s_cbranch_vccnz .LBB0_1174
	s_waitcnt vmcnt(0)
	v_lshlrev_b32_e32 v156, 16, v156
	v_lshlrev_b32_e32 v158, 16, v158
	v_lshlrev_b32_e32 v159, 16, v159
	v_lshlrev_b32_e32 v157, 16, v157
	v_lshlrev_b32_e32 v162, 16, v162
	v_lshlrev_b32_e32 v163, 16, v163
	v_lshlrev_b32_e32 v161, 16, v161
	v_lshlrev_b32_e32 v160, 16, v160
	v_lshlrev_b32_e32 v165, 16, v165
	v_lshlrev_b32_e32 v164, 16, v164
	v_lshlrev_b32_e32 v171, 16, v171
	v_lshlrev_b32_e32 v170, 16, v170
	v_lshlrev_b32_e32 v169, 16, v169
	v_lshlrev_b32_e32 v168, 16, v168
	v_lshlrev_b32_e32 v167, 16, v167
	v_lshlrev_b32_e32 v166, 16, v166

; __global__ void __launch_bounds__(512, 2) mk_fwd(Args args) {
	.amdhsa_kernel _Z6mk_fwd4Args
		.amdhsa_group_segment_fixed_size 0
		.amdhsa_private_segment_fixed_size 0
		.amdhsa_kernarg_size 520
		.amdhsa_user_sgpr_count 2
		.amdhsa_user_sgpr_dispatch_ptr 0
		.amdhsa_user_sgpr_queue_ptr 0
		.amdhsa_user_sgpr_kernarg_segment_ptr 1
		.amdhsa_user_sgpr_dispatch_id 0
		.amdhsa_user_sgpr_kernarg_preload_length 0
		.amdhsa_user_sgpr_kernarg_preload_offset 0
		.amdhsa_user_sgpr_private_segment_size 0
		.amdhsa_uses_dynamic_stack 0
		.amdhsa_enable_private_segment 0
		.amdhsa_system_sgpr_workgroup_id_x 1
		.amdhsa_system_sgpr_workgroup_id_y 0
		.amdhsa_system_sgpr_workgroup_id_z 0
		.amdhsa_system_sgpr_workgroup_info 0
		.amdhsa_system_vgpr_workitem_id 0
		.amdhsa_next_free_vgpr 256
		.amdhsa_next_free_sgpr 102
		.amdhsa_accum_offset 256
		.amdhsa_reserve_vcc 1
		.amdhsa_float_round_mode_32 0
		.amdhsa_float_round_mode_16_64 0
		.amdhsa_float_denorm_mode_32 3
		.amdhsa_float_denorm_mode_16_64 3
		.amdhsa_dx10_clamp 1
		.amdhsa_ieee_mode 1
		.amdhsa_fp16_overflow 0
		.amdhsa_tg_split 0
		.amdhsa_exception_fp_ieee_invalid_op 0
		.amdhsa_exception_fp_denorm_src 0
		.amdhsa_exception_fp_ieee_div_zero 0
		.amdhsa_exception_fp_ieee_overflow 0
		.amdhsa_exception_fp_ieee_underflow 0
		.amdhsa_exception_fp_ieee_inexact 0
		.amdhsa_exception_int_div_zero 0
	.end_amdhsa_kernel

; __global__ void __launch_bounds__(512, 2) mk_fwd(Args args) {
amdhsa.kernels:
  - .agpr_count:     0
    .args:
      - .offset:         0
        .size:           264
        .value_kind:     by_value
      - .offset:         264
        .size:           4
        .value_kind:     hidden_block_count_x
      - .offset:         268
        .size:           4
        .value_kind:     hidden_block_count_y
      - .offset:         272
        .size:           4
        .value_kind:     hidden_block_count_z
      - .offset:         276
        .size:           2
        .value_kind:     hidden_group_size_x
      - .offset:         278
        .size:           2
        .value_kind:     hidden_group_size_y
      - .offset:         280
        .size:           2
        .value_kind:     hidden_group_size_z
      - .offset:         282
        .size:           2
        .value_kind:     hidden_remainder_x
      - .offset:         284
        .size:           2
        .value_kind:     hidden_remainder_y
      - .offset:         286
        .size:           2
        .value_kind:     hidden_remainder_z
      - .offset:         304
        .size:           8
        .value_kind:     hidden_global_offset_x
      - .offset:         312
        .size:           8
        .value_kind:     hidden_global_offset_y
      - .offset:         320
        .size:           8
        .value_kind:     hidden_global_offset_z
      - .offset:         328
        .size:           2
        .value_kind:     hidden_grid_dims
      - .offset:         384
        .size:           4
        .value_kind:     hidden_dynamic_lds_size
    .group_segment_fixed_size: 0
    .kernarg_segment_align: 8
    .kernarg_segment_size: 520
    .language:       OpenCL C
    .language_version:
      - 2
      - 0
    .max_flat_workgroup_size: 512
    .name:           _Z6mk_fwd4Args
    .private_segment_fixed_size: 0
    .sgpr_count:     108
    .sgpr_spill_count: 331
    .symbol:         _Z6mk_fwd4Args.kd
    .uniform_work_group_size: 1
    .uses_dynamic_stack: false
    .vgpr_count:     256
    .vgpr_spill_count: 0
    .wavefront_size: 64
